# P1 tail: LORAT / WPOOLT bf16 weight copies rewritten as straight-line code with all 22 loads of a lane in flight (was one element per iteration behind vmcnt(0))
# speedup vs baseline: 1.0063x; 1.0005x over previous
; __device__ __forceinline__ unsigned f2bf(float f) { return cvt_pk_bf16_nat(f, 0.f) & 0xffffu; }
; __global__ void __launch_bounds__(NTHR, 2) mk_fwd(Args args) {
;     ...
;         for (int i = hw * 64 + lane; i < 3072 * LK; i += HW * 64) {
;             const int n = i / LK, k = i % LK; float v = 0.f;
;             if (n < 1024) { if (k < 64) v = w2d[k * 1024 + n]; }
;             else if (n < 2048) { if (k >= 64 && k < 128) v = a2[(k - 64) * 1024 + (n - 1024)]; }
;             else { if (k >= 128 && k < 288) v = g2[(k - 128) * 1024 + (n - 2048)]; }
;             LORAT[i] = (bf16)f2bf(v);
;         }
.LBB0_105:
	v_lshl_or_b32 v2, s0, 6, v194
	v_readlane_b32 s36, v252, 8
	v_readlane_b32 s37, v252, 9
	v_readlane_b32 s38, v252, 12
	v_readlane_b32 s39, v252, 13
	v_readlane_b32 s40, v252, 14
	v_readlane_b32 s41, v252, 15
	v_mov_b32_e32 v3, 0
	v_mov_b32_e32 v4, 0xaaab
	v_mov_b32_e32 v5, 0x180
	v_mov_b32_e32 v6, s38
	v_mov_b32_e32 v7, s39
	v_mov_b32_e32 v8, s40
	v_mov_b32_e32 v9, s41
	v_mov_b32_e32 v10, 64
	v_mov_b32_e32 v11, 0x80
	v_mov_b32_e32 v12, 0xa0
	v_mov_b32_e32 v13, v2
	v_lshrrev_b32_e32 v14, 7, v13
	v_mul_u32_u24_e32 v14, v14, v4
	v_lshrrev_b32_e32 v14, 17, v14
	v_mul_u32_u24_e32 v15, v14, v5
	v_sub_u32_e32 v15, v13, v15
	v_and_b32_e32 v16, 0x3ff, v14
	v_cmp_lt_u32_e32 vcc, 0x3ff, v14
	v_mov_b32_e32 v18, s36
	v_mov_b32_e32 v19, s37
	v_cndmask_b32_e32 v17, 0, v10, vcc
	v_cndmask_b32_e32 v18, v18, v6, vcc
	v_cndmask_b32_e32 v19, v19, v7, vcc
	v_cmp_lt_u32_e32 vcc, 0x7ff, v14
	s_nop 1
	v_cndmask_b32_e32 v17, v17, v11, vcc
	v_cndmask_b32_e32 v20, v10, v12, vcc
	v_cndmask_b32_e32 v18, v18, v8, vcc
	v_cndmask_b32_e32 v19, v19, v9, vcc
	v_sub_u32_e32 v15, v15, v17
	v_cmp_lt_u32_e32 vcc, v15, v20
	v_lshl_add_u32 v15, v15, 10, v16
	v_mov_b32_e32 v23, 0
	v_cndmask_b32_e32 v22, 0, v15, vcc
	v_cndmask_b32_e64 v120, 0, -1, vcc
	v_lshl_add_u64 v[18:19], v[22:23], 2, v[18:19]
	global_load_dword v100, v[18:19], off
	v_add_u32_e32 v13, 65536, v2
	v_lshrrev_b32_e32 v14, 7, v13
	v_mul_u32_u24_e32 v14, v14, v4
	v_lshrrev_b32_e32 v14, 17, v14
	v_mul_u32_u24_e32 v15, v14, v5
	v_sub_u32_e32 v15, v13, v15
	v_and_b32_e32 v16, 0x3ff, v14
	v_cmp_lt_u32_e32 vcc, 0x3ff, v14
	v_mov_b32_e32 v18, s36
	v_mov_b32_e32 v19, s37
	v_cndmask_b32_e32 v17, 0, v10, vcc
	v_cndmask_b32_e32 v18, v18, v6, vcc
	v_cndmask_b32_e32 v19, v19, v7, vcc
	v_cmp_lt_u32_e32 vcc, 0x7ff, v14
	s_nop 1
	v_cndmask_b32_e32 v17, v17, v11, vcc
	v_cndmask_b32_e32 v20, v10, v12, vcc
	v_cndmask_b32_e32 v18, v18, v8, vcc
	v_cndmask_b32_e32 v19, v19, v9, vcc
	v_sub_u32_e32 v15, v15, v17
	v_cmp_lt_u32_e32 vcc, v15, v20
	v_lshl_add_u32 v15, v15, 10, v16
	v_mov_b32_e32 v23, 0
	v_cndmask_b32_e32 v22, 0, v15, vcc
	v_cndmask_b32_e64 v121, 0, -1, vcc
	v_lshl_add_u64 v[18:19], v[22:23], 2, v[18:19]
	global_load_dword v101, v[18:19], off
	v_add_u32_e32 v13, 131072, v2
	v_lshrrev_b32_e32 v14, 7, v13
	v_mul_u32_u24_e32 v14, v14, v4
	v_lshrrev_b32_e32 v14, 17, v14
	v_mul_u32_u24_e32 v15, v14, v5
	v_sub_u32_e32 v15, v13, v15
	v_and_b32_e32 v16, 0x3ff, v14
	v_cmp_lt_u32_e32 vcc, 0x3ff, v14
	v_mov_b32_e32 v18, s36
	v_mov_b32_e32 v19, s37
	v_cndmask_b32_e32 v17, 0, v10, vcc
	v_cndmask_b32_e32 v18, v18, v6, vcc
	v_cndmask_b32_e32 v19, v19, v7, vcc
	v_cmp_lt_u32_e32 vcc, 0x7ff, v14
	s_nop 1
	v_cndmask_b32_e32 v17, v17, v11, vcc
	v_cndmask_b32_e32 v20, v10, v12, vcc
	v_cndmask_b32_e32 v18, v18, v8, vcc
	v_cndmask_b32_e32 v19, v19, v9, vcc
	v_sub_u32_e32 v15, v15, v17
	v_cmp_lt_u32_e32 vcc, v15, v20
	v_lshl_add_u32 v15, v15, 10, v16
	v_mov_b32_e32 v23, 0
	v_cndmask_b32_e32 v22, 0, v15, vcc
	v_cndmask_b32_e64 v122, 0, -1, vcc
	v_lshl_add_u64 v[18:19], v[22:23], 2, v[18:19]
	global_load_dword v102, v[18:19], off
	v_add_u32_e32 v13, 196608, v2
	v_lshrrev_b32_e32 v14, 7, v13
	v_mul_u32_u24_e32 v14, v14, v4
	v_lshrrev_b32_e32 v14, 17, v14
	v_mul_u32_u24_e32 v15, v14, v5
	v_sub_u32_e32 v15, v13, v15
	v_and_b32_e32 v16, 0x3ff, v14
	v_cmp_lt_u32_e32 vcc, 0x3ff, v14
	v_mov_b32_e32 v18, s36
	v_mov_b32_e32 v19, s37
	v_cndmask_b32_e32 v17, 0, v10, vcc
	v_cndmask_b32_e32 v18, v18, v6, vcc
	v_cndmask_b32_e32 v19, v19, v7, vcc
	v_cmp_lt_u32_e32 vcc, 0x7ff, v14
	s_nop 1
	v_cndmask_b32_e32 v17, v17, v11, vcc
	v_cndmask_b32_e32 v20, v10, v12, vcc
	v_cndmask_b32_e32 v18, v18, v8, vcc
	v_cndmask_b32_e32 v19, v19, v9, vcc
	v_sub_u32_e32 v15, v15, v17
	v_cmp_lt_u32_e32 vcc, v15, v20
	v_lshl_add_u32 v15, v15, 10, v16
	v_mov_b32_e32 v23, 0
	v_cndmask_b32_e32 v22, 0, v15, vcc
	v_cndmask_b32_e64 v123, 0, -1, vcc
	v_lshl_add_u64 v[18:19], v[22:23], 2, v[18:19]
	global_load_dword v103, v[18:19], off
	v_add_u32_e32 v13, 262144, v2
	v_lshrrev_b32_e32 v14, 7, v13
	v_mul_u32_u24_e32 v14, v14, v4
	v_lshrrev_b32_e32 v14, 17, v14
	v_mul_u32_u24_e32 v15, v14, v5
	v_sub_u32_e32 v15, v13, v15
	v_and_b32_e32 v16, 0x3ff, v14
	v_cmp_lt_u32_e32 vcc, 0x3ff, v14
	v_mov_b32_e32 v18, s36
	v_mov_b32_e32 v19, s37
	v_cndmask_b32_e32 v17, 0, v10, vcc
	v_cndmask_b32_e32 v18, v18, v6, vcc
	v_cndmask_b32_e32 v19, v19, v7, vcc
	v_cmp_lt_u32_e32 vcc, 0x7ff, v14
	s_nop 1
	v_cndmask_b32_e32 v17, v17, v11, vcc
	v_cndmask_b32_e32 v20, v10, v12, vcc
	v_cndmask_b32_e32 v18, v18, v8, vcc
	v_cndmask_b32_e32 v19, v19, v9, vcc
	v_sub_u32_e32 v15, v15, v17
	v_cmp_lt_u32_e32 vcc, v15, v20
	v_lshl_add_u32 v15, v15, 10, v16
	v_mov_b32_e32 v23, 0
	v_cndmask_b32_e32 v22, 0, v15, vcc
	v_cndmask_b32_e64 v124, 0, -1, vcc
	v_lshl_add_u64 v[18:19], v[22:23], 2, v[18:19]
	global_load_dword v104, v[18:19], off
	v_add_u32_e32 v13, 327680, v2
	v_lshrrev_b32_e32 v14, 7, v13
	v_mul_u32_u24_e32 v14, v14, v4
	v_lshrrev_b32_e32 v14, 17, v14
	v_mul_u32_u24_e32 v15, v14, v5
	v_sub_u32_e32 v15, v13, v15
	v_and_b32_e32 v16, 0x3ff, v14
	v_cmp_lt_u32_e32 vcc, 0x3ff, v14
	v_mov_b32_e32 v18, s36
	v_mov_b32_e32 v19, s37
	v_cndmask_b32_e32 v17, 0, v10, vcc
	v_cndmask_b32_e32 v18, v18, v6, vcc
	v_cndmask_b32_e32 v19, v19, v7, vcc
	v_cmp_lt_u32_e32 vcc, 0x7ff, v14
	s_nop 1
	v_cndmask_b32_e32 v17, v17, v11, vcc
	v_cndmask_b32_e32 v20, v10, v12, vcc
	v_cndmask_b32_e32 v18, v18, v8, vcc
	v_cndmask_b32_e32 v19, v19, v9, vcc
	v_sub_u32_e32 v15, v15, v17
	v_cmp_lt_u32_e32 vcc, v15, v20
	v_lshl_add_u32 v15, v15, 10, v16
	v_mov_b32_e32 v23, 0
	v_cndmask_b32_e32 v22, 0, v15, vcc
	v_cndmask_b32_e64 v125, 0, -1, vcc
; __device__ __forceinline__ unsigned f2bf(float f) { return cvt_pk_bf16_nat(f, 0.f) & 0xffffu; }
; __global__ void __launch_bounds__(NTHR, 2) mk_fwd(Args args) {
;     ...
;         for (int i = hw * 64 + lane; i < 3072 * LK; i += HW * 64) {
;             const int n = i / LK, k = i % LK; float v = 0.f;
;             if (n < 1024) { if (k < 64) v = w2d[k * 1024 + n]; }
;             else if (n < 2048) { if (k >= 64 && k < 128) v = a2[(k - 64) * 1024 + (n - 1024)]; }
;             else { if (k >= 128 && k < 288) v = g2[(k - 128) * 1024 + (n - 2048)]; }
;             LORAT[i] = (bf16)f2bf(v);
	v_lshl_add_u64 v[18:19], v[22:23], 2, v[18:19]
	global_load_dword v105, v[18:19], off
	v_add_u32_e32 v13, 393216, v2
	v_lshrrev_b32_e32 v14, 7, v13
	v_mul_u32_u24_e32 v14, v14, v4
	v_lshrrev_b32_e32 v14, 17, v14
	v_mul_u32_u24_e32 v15, v14, v5
	v_sub_u32_e32 v15, v13, v15
	v_and_b32_e32 v16, 0x3ff, v14
	v_cmp_lt_u32_e32 vcc, 0x3ff, v14
	v_mov_b32_e32 v18, s36
	v_mov_b32_e32 v19, s37
	v_cndmask_b32_e32 v17, 0, v10, vcc
	v_cndmask_b32_e32 v18, v18, v6, vcc
	v_cndmask_b32_e32 v19, v19, v7, vcc
	v_cmp_lt_u32_e32 vcc, 0x7ff, v14
	s_nop 1
	v_cndmask_b32_e32 v17, v17, v11, vcc
	v_cndmask_b32_e32 v20, v10, v12, vcc
	v_cndmask_b32_e32 v18, v18, v8, vcc
	v_cndmask_b32_e32 v19, v19, v9, vcc
	v_sub_u32_e32 v15, v15, v17
	v_cmp_lt_u32_e32 vcc, v15, v20
	v_lshl_add_u32 v15, v15, 10, v16
	v_mov_b32_e32 v23, 0
	v_cndmask_b32_e32 v22, 0, v15, vcc
	v_cndmask_b32_e64 v126, 0, -1, vcc
	v_lshl_add_u64 v[18:19], v[22:23], 2, v[18:19]
	global_load_dword v106, v[18:19], off
	v_add_u32_e32 v13, 458752, v2
	v_lshrrev_b32_e32 v14, 7, v13
	v_mul_u32_u24_e32 v14, v14, v4
	v_lshrrev_b32_e32 v14, 17, v14
	v_mul_u32_u24_e32 v15, v14, v5
	v_sub_u32_e32 v15, v13, v15
	v_and_b32_e32 v16, 0x3ff, v14
	v_cmp_lt_u32_e32 vcc, 0x3ff, v14
	v_mov_b32_e32 v18, s36
	v_mov_b32_e32 v19, s37
	v_cndmask_b32_e32 v17, 0, v10, vcc
	v_cndmask_b32_e32 v18, v18, v6, vcc
	v_cndmask_b32_e32 v19, v19, v7, vcc
	v_cmp_lt_u32_e32 vcc, 0x7ff, v14
	s_nop 1
	v_cndmask_b32_e32 v17, v17, v11, vcc
	v_cndmask_b32_e32 v20, v10, v12, vcc
	v_cndmask_b32_e32 v18, v18, v8, vcc
	v_cndmask_b32_e32 v19, v19, v9, vcc
	v_sub_u32_e32 v15, v15, v17
	v_cmp_lt_u32_e32 vcc, v15, v20
	v_lshl_add_u32 v15, v15, 10, v16
	v_mov_b32_e32 v23, 0
	v_cndmask_b32_e32 v22, 0, v15, vcc
	v_cndmask_b32_e64 v127, 0, -1, vcc
	v_lshl_add_u64 v[18:19], v[22:23], 2, v[18:19]
	global_load_dword v107, v[18:19], off
	v_add_u32_e32 v13, 524288, v2
	v_lshrrev_b32_e32 v14, 7, v13
	v_mul_u32_u24_e32 v14, v14, v4
	v_lshrrev_b32_e32 v14, 17, v14
	v_mul_u32_u24_e32 v15, v14, v5
	v_sub_u32_e32 v15, v13, v15
	v_and_b32_e32 v16, 0x3ff, v14
	v_cmp_lt_u32_e32 vcc, 0x3ff, v14
	v_mov_b32_e32 v18, s36
	v_mov_b32_e32 v19, s37
	v_cndmask_b32_e32 v17, 0, v10, vcc
	v_cndmask_b32_e32 v18, v18, v6, vcc
	v_cndmask_b32_e32 v19, v19, v7, vcc
	v_cmp_lt_u32_e32 vcc, 0x7ff, v14
	s_nop 1
	v_cndmask_b32_e32 v17, v17, v11, vcc
	v_cndmask_b32_e32 v20, v10, v12, vcc
	v_cndmask_b32_e32 v18, v18, v8, vcc
	v_cndmask_b32_e32 v19, v19, v9, vcc
	v_sub_u32_e32 v15, v15, v17
	v_cmp_lt_u32_e32 vcc, v15, v20
	v_lshl_add_u32 v15, v15, 10, v16
	v_mov_b32_e32 v23, 0
	v_cndmask_b32_e32 v22, 0, v15, vcc
	v_cndmask_b32_e64 v128, 0, -1, vcc
	v_lshl_add_u64 v[18:19], v[22:23], 2, v[18:19]
	global_load_dword v108, v[18:19], off
	v_add_u32_e32 v13, 589824, v2
	v_lshrrev_b32_e32 v14, 7, v13
	v_mul_u32_u24_e32 v14, v14, v4
	v_lshrrev_b32_e32 v14, 17, v14
	v_mul_u32_u24_e32 v15, v14, v5
	v_sub_u32_e32 v15, v13, v15
	v_and_b32_e32 v16, 0x3ff, v14
	v_cmp_lt_u32_e32 vcc, 0x3ff, v14
	v_mov_b32_e32 v18, s36
	v_mov_b32_e32 v19, s37
	v_cndmask_b32_e32 v17, 0, v10, vcc
	v_cndmask_b32_e32 v18, v18, v6, vcc
	v_cndmask_b32_e32 v19, v19, v7, vcc
	v_cmp_lt_u32_e32 vcc, 0x7ff, v14
	s_nop 1
	v_cndmask_b32_e32 v17, v17, v11, vcc
	v_cndmask_b32_e32 v20, v10, v12, vcc
	v_cndmask_b32_e32 v18, v18, v8, vcc
	v_cndmask_b32_e32 v19, v19, v9, vcc
	v_sub_u32_e32 v15, v15, v17
	v_cmp_lt_u32_e32 vcc, v15, v20
	v_lshl_add_u32 v15, v15, 10, v16
	v_mov_b32_e32 v23, 0
	v_cndmask_b32_e32 v22, 0, v15, vcc
	v_cndmask_b32_e64 v129, 0, -1, vcc
	v_lshl_add_u64 v[18:19], v[22:23], 2, v[18:19]
	global_load_dword v109, v[18:19], off
	v_add_u32_e32 v13, 655360, v2
	v_lshrrev_b32_e32 v14, 7, v13
	v_mul_u32_u24_e32 v14, v14, v4
	v_lshrrev_b32_e32 v14, 17, v14
	v_mul_u32_u24_e32 v15, v14, v5
	v_sub_u32_e32 v15, v13, v15
	v_and_b32_e32 v16, 0x3ff, v14
	v_cmp_lt_u32_e32 vcc, 0x3ff, v14
	v_mov_b32_e32 v18, s36
	v_mov_b32_e32 v19, s37
	v_cndmask_b32_e32 v17, 0, v10, vcc
	v_cndmask_b32_e32 v18, v18, v6, vcc
	v_cndmask_b32_e32 v19, v19, v7, vcc
	v_cmp_lt_u32_e32 vcc, 0x7ff, v14
	s_nop 1
	v_cndmask_b32_e32 v17, v17, v11, vcc
	v_cndmask_b32_e32 v20, v10, v12, vcc
	v_cndmask_b32_e32 v18, v18, v8, vcc
	v_cndmask_b32_e32 v19, v19, v9, vcc
	v_sub_u32_e32 v15, v15, v17
	v_cmp_lt_u32_e32 vcc, v15, v20
	v_lshl_add_u32 v15, v15, 10, v16
	v_mov_b32_e32 v23, 0
	v_cndmask_b32_e32 v22, 0, v15, vcc
	v_cndmask_b32_e64 v130, 0, -1, vcc
	v_lshl_add_u64 v[18:19], v[22:23], 2, v[18:19]
	global_load_dword v110, v[18:19], off
	v_add_u32_e32 v13, 720896, v2
	v_lshrrev_b32_e32 v14, 7, v13
	v_mul_u32_u24_e32 v14, v14, v4
	v_lshrrev_b32_e32 v14, 17, v14
	v_mul_u32_u24_e32 v15, v14, v5
	v_sub_u32_e32 v15, v13, v15
	v_and_b32_e32 v16, 0x3ff, v14
	v_cmp_lt_u32_e32 vcc, 0x3ff, v14
	v_mov_b32_e32 v18, s36
	v_mov_b32_e32 v19, s37
	v_cndmask_b32_e32 v17, 0, v10, vcc
	v_cndmask_b32_e32 v18, v18, v6, vcc
	v_cndmask_b32_e32 v19, v19, v7, vcc
	v_cmp_lt_u32_e32 vcc, 0x7ff, v14
	s_nop 1
	v_cndmask_b32_e32 v17, v17, v11, vcc
	v_cndmask_b32_e32 v20, v10, v12, vcc
	v_cndmask_b32_e32 v18, v18, v8, vcc
	v_cndmask_b32_e32 v19, v19, v9, vcc
	v_sub_u32_e32 v15, v15, v17
	v_cmp_lt_u32_e32 vcc, v15, v20
	v_lshl_add_u32 v15, v15, 10, v16
	v_mov_b32_e32 v23, 0
	v_cndmask_b32_e32 v22, 0, v15, vcc
	v_cndmask_b32_e64 v131, 0, -1, vcc
	v_lshl_add_u64 v[18:19], v[22:23], 2, v[18:19]
	global_load_dword v111, v[18:19], off
	v_add_u32_e32 v13, 786432, v2
	v_lshrrev_b32_e32 v14, 7, v13
	v_mul_u32_u24_e32 v14, v14, v4
	v_lshrrev_b32_e32 v14, 17, v14
	v_mul_u32_u24_e32 v15, v14, v5
	v_sub_u32_e32 v15, v13, v15
	v_and_b32_e32 v16, 0x3ff, v14
	v_cmp_lt_u32_e32 vcc, 0x3ff, v14
	v_mov_b32_e32 v18, s36
; __device__ __forceinline__ unsigned f2bf(float f) { return cvt_pk_bf16_nat(f, 0.f) & 0xffffu; }
; __global__ void __launch_bounds__(NTHR, 2) mk_fwd(Args args) {
;     ...
;         for (int i = hw * 64 + lane; i < 3072 * LK; i += HW * 64) {
;             const int n = i / LK, k = i % LK; float v = 0.f;
;             if (n < 1024) { if (k < 64) v = w2d[k * 1024 + n]; }
;             else if (n < 2048) { if (k >= 64 && k < 128) v = a2[(k - 64) * 1024 + (n - 1024)]; }
;             else { if (k >= 128 && k < 288) v = g2[(k - 128) * 1024 + (n - 2048)]; }
;             LORAT[i] = (bf16)f2bf(v);
;         }
;         for (int i = hw * 64 + lane; i < 1024 * 256; i += HW * 64) {
;             const int n = i >> 8, c = i & 255, g = n >> 8, d = n & 255;
;             WPOOLT[i] = (bf16)f2bf(w_pool[((size_t)g * 256 + c) * 256 + d]);
	v_mov_b32_e32 v19, s37
	v_cndmask_b32_e32 v17, 0, v10, vcc
	v_cndmask_b32_e32 v18, v18, v6, vcc
	v_cndmask_b32_e32 v19, v19, v7, vcc
	v_cmp_lt_u32_e32 vcc, 0x7ff, v14
	s_nop 1
	v_cndmask_b32_e32 v17, v17, v11, vcc
	v_cndmask_b32_e32 v20, v10, v12, vcc
	v_cndmask_b32_e32 v18, v18, v8, vcc
	v_cndmask_b32_e32 v19, v19, v9, vcc
	v_sub_u32_e32 v15, v15, v17
	v_cmp_lt_u32_e32 vcc, v15, v20
	v_lshl_add_u32 v15, v15, 10, v16
	v_mov_b32_e32 v23, 0
	v_cndmask_b32_e32 v22, 0, v15, vcc
	v_cndmask_b32_e64 v132, 0, -1, vcc
	v_lshl_add_u64 v[18:19], v[22:23], 2, v[18:19]
	global_load_dword v112, v[18:19], off
	v_add_u32_e32 v13, 851968, v2
	v_lshrrev_b32_e32 v14, 7, v13
	v_mul_u32_u24_e32 v14, v14, v4
	v_lshrrev_b32_e32 v14, 17, v14
	v_mul_u32_u24_e32 v15, v14, v5
	v_sub_u32_e32 v15, v13, v15
	v_and_b32_e32 v16, 0x3ff, v14
	v_cmp_lt_u32_e32 vcc, 0x3ff, v14
	v_mov_b32_e32 v18, s36
	v_mov_b32_e32 v19, s37
	v_cndmask_b32_e32 v17, 0, v10, vcc
	v_cndmask_b32_e32 v18, v18, v6, vcc
	v_cndmask_b32_e32 v19, v19, v7, vcc
	v_cmp_lt_u32_e32 vcc, 0x7ff, v14
	s_nop 1
	v_cndmask_b32_e32 v17, v17, v11, vcc
	v_cndmask_b32_e32 v20, v10, v12, vcc
	v_cndmask_b32_e32 v18, v18, v8, vcc
	v_cndmask_b32_e32 v19, v19, v9, vcc
	v_sub_u32_e32 v15, v15, v17
	v_cmp_lt_u32_e32 vcc, v15, v20
	v_lshl_add_u32 v15, v15, 10, v16
	v_mov_b32_e32 v23, 0
	v_cndmask_b32_e32 v22, 0, v15, vcc
	v_cndmask_b32_e64 v133, 0, -1, vcc
	v_lshl_add_u64 v[18:19], v[22:23], 2, v[18:19]
	global_load_dword v113, v[18:19], off
	v_add_u32_e32 v13, 917504, v2
	v_lshrrev_b32_e32 v14, 7, v13
	v_mul_u32_u24_e32 v14, v14, v4
	v_lshrrev_b32_e32 v14, 17, v14
	v_mul_u32_u24_e32 v15, v14, v5
	v_sub_u32_e32 v15, v13, v15
	v_and_b32_e32 v16, 0x3ff, v14
	v_cmp_lt_u32_e32 vcc, 0x3ff, v14
	v_mov_b32_e32 v18, s36
	v_mov_b32_e32 v19, s37
	v_cndmask_b32_e32 v17, 0, v10, vcc
	v_cndmask_b32_e32 v18, v18, v6, vcc
	v_cndmask_b32_e32 v19, v19, v7, vcc
	v_cmp_lt_u32_e32 vcc, 0x7ff, v14
	s_nop 1
	v_cndmask_b32_e32 v17, v17, v11, vcc
	v_cndmask_b32_e32 v20, v10, v12, vcc
	v_cndmask_b32_e32 v18, v18, v8, vcc
	v_cndmask_b32_e32 v19, v19, v9, vcc
	v_sub_u32_e32 v15, v15, v17
	v_cmp_lt_u32_e32 vcc, v15, v20
	v_lshl_add_u32 v15, v15, 10, v16
	v_mov_b32_e32 v23, 0
	v_cndmask_b32_e32 v22, 0, v15, vcc
	v_cndmask_b32_e64 v134, 0, -1, vcc
	v_lshl_add_u64 v[18:19], v[22:23], 2, v[18:19]
	global_load_dword v114, v[18:19], off
	v_add_u32_e32 v13, 983040, v2
	v_lshrrev_b32_e32 v14, 7, v13
	v_mul_u32_u24_e32 v14, v14, v4
	v_lshrrev_b32_e32 v14, 17, v14
	v_mul_u32_u24_e32 v15, v14, v5
	v_sub_u32_e32 v15, v13, v15
	v_and_b32_e32 v16, 0x3ff, v14
	v_cmp_lt_u32_e32 vcc, 0x3ff, v14
	v_mov_b32_e32 v18, s36
	v_mov_b32_e32 v19, s37
	v_cndmask_b32_e32 v17, 0, v10, vcc
	v_cndmask_b32_e32 v18, v18, v6, vcc
	v_cndmask_b32_e32 v19, v19, v7, vcc
	v_cmp_lt_u32_e32 vcc, 0x7ff, v14
	s_nop 1
	v_cndmask_b32_e32 v17, v17, v11, vcc
	v_cndmask_b32_e32 v20, v10, v12, vcc
	v_cndmask_b32_e32 v18, v18, v8, vcc
	v_cndmask_b32_e32 v19, v19, v9, vcc
	v_sub_u32_e32 v15, v15, v17
	v_cmp_lt_u32_e32 vcc, v15, v20
	v_lshl_add_u32 v15, v15, 10, v16
	v_mov_b32_e32 v23, 0
	v_cndmask_b32_e32 v22, 0, v15, vcc
	v_cndmask_b32_e64 v135, 0, -1, vcc
	v_lshl_add_u64 v[18:19], v[22:23], 2, v[18:19]
	global_load_dword v115, v[18:19], off
	v_add_u32_e32 v13, 1048576, v2
	v_lshrrev_b32_e32 v14, 7, v13
	v_mul_u32_u24_e32 v14, v14, v4
	v_lshrrev_b32_e32 v14, 17, v14
	v_mul_u32_u24_e32 v15, v14, v5
	v_sub_u32_e32 v15, v13, v15
	v_and_b32_e32 v16, 0x3ff, v14
	v_cmp_lt_u32_e32 vcc, 0x3ff, v14
	v_mov_b32_e32 v18, s36
	v_mov_b32_e32 v19, s37
	v_cndmask_b32_e32 v17, 0, v10, vcc
	v_cndmask_b32_e32 v18, v18, v6, vcc
	v_cndmask_b32_e32 v19, v19, v7, vcc
	v_cmp_lt_u32_e32 vcc, 0x7ff, v14
	s_nop 1
	v_cndmask_b32_e32 v17, v17, v11, vcc
	v_cndmask_b32_e32 v20, v10, v12, vcc
	v_cndmask_b32_e32 v18, v18, v8, vcc
	v_cndmask_b32_e32 v19, v19, v9, vcc
	v_sub_u32_e32 v15, v15, v17
	v_cmp_lt_u32_e32 vcc, v15, v20
	v_lshl_add_u32 v15, v15, 10, v16
	v_mov_b32_e32 v23, 0
	v_cndmask_b32_e32 v22, 0, v15, vcc
	v_cndmask_b32_e64 v136, 0, -1, vcc
	v_lshl_add_u64 v[18:19], v[22:23], 2, v[18:19]
	global_load_dword v116, v[18:19], off
	v_add_u32_e32 v13, 1114112, v2
	v_lshrrev_b32_e32 v14, 7, v13
	v_mul_u32_u24_e32 v14, v14, v4
	v_lshrrev_b32_e32 v14, 17, v14
	v_mul_u32_u24_e32 v15, v14, v5
	v_sub_u32_e32 v15, v13, v15
	v_and_b32_e32 v16, 0x3ff, v14
	v_cmp_lt_u32_e32 vcc, 0x3ff, v14
	v_mov_b32_e32 v18, s36
	v_mov_b32_e32 v19, s37
	v_cndmask_b32_e32 v17, 0, v10, vcc
	v_cndmask_b32_e32 v18, v18, v6, vcc
	v_cndmask_b32_e32 v19, v19, v7, vcc
	v_cmp_lt_u32_e32 vcc, 0x7ff, v14
	s_nop 1
	v_cndmask_b32_e32 v17, v17, v11, vcc
	v_cndmask_b32_e32 v20, v10, v12, vcc
	v_cndmask_b32_e32 v18, v18, v8, vcc
	v_cndmask_b32_e32 v19, v19, v9, vcc
	v_sub_u32_e32 v15, v15, v17
	v_cmp_lt_u32_e32 vcc, v15, v20
	v_lshl_add_u32 v15, v15, 10, v16
	v_mov_b32_e32 v23, 0
	v_cndmask_b32_e32 v22, 0, v15, vcc
	v_cndmask_b32_e64 v137, 0, -1, vcc
	v_lshl_add_u64 v[18:19], v[22:23], 2, v[18:19]
	global_load_dword v117, v[18:19], off
	v_mov_b32_e32 v13, v2
	v_lshrrev_b32_e32 v14, 8, v13
	v_and_b32_e32 v15, 0xff, v13
	v_and_b32_e32 v16, 0xff, v14
	v_and_b32_e32 v14, 0x300, v14
	v_or_b32_e32 v14, v14, v15
	v_lshl_or_b32 v22, v14, 8, v16
	v_mov_b32_e32 v23, 0
	v_lshl_add_u64 v[18:19], v[22:23], 2, s[62:63]
	global_load_dword v140, v[18:19], off
	v_add_u32_e32 v13, 65536, v2
	v_lshrrev_b32_e32 v14, 8, v13
	v_and_b32_e32 v15, 0xff, v13
	v_and_b32_e32 v16, 0xff, v14
	v_and_b32_e32 v14, 0x300, v14
	v_or_b32_e32 v14, v14, v15
	v_lshl_or_b32 v22, v14, 8, v16
	v_mov_b32_e32 v23, 0
	v_lshl_add_u64 v[18:19], v[22:23], 2, s[62:63]
	global_load_dword v141, v[18:19], off
	v_add_u32_e32 v13, 131072, v2
	v_lshrrev_b32_e32 v14, 8, v13
	v_and_b32_e32 v15, 0xff, v13
	v_and_b32_e32 v16, 0xff, v14
	v_and_b32_e32 v14, 0x300, v14
	v_or_b32_e32 v14, v14, v15
	v_lshl_or_b32 v22, v14, 8, v16
	v_mov_b32_e32 v23, 0
	v_lshl_add_u64 v[18:19], v[22:23], 2, s[62:63]
	global_load_dword v142, v[18:19], off
	v_add_u32_e32 v13, 196608, v2
	v_lshrrev_b32_e32 v14, 8, v13
	v_and_b32_e32 v15, 0xff, v13
	v_and_b32_e32 v16, 0xff, v14
	v_and_b32_e32 v14, 0x300, v14
	v_or_b32_e32 v14, v14, v15
	v_lshl_or_b32 v22, v14, 8, v16
	v_mov_b32_e32 v23, 0
	v_lshl_add_u64 v[18:19], v[22:23], 2, s[62:63]
	global_load_dword v143, v[18:19], off
	v_lshlrev_b32_e32 v22, 1, v2
	v_mov_b32_e32 v23, 0
	s_add_u32 s6, s26, 0x5d48000
	s_addc_u32 s7, s27, 0
	v_lshl_add_u64 v[24:25], s[6:7], 0, v[22:23]
	v_lshl_add_u64 v[26:27], s[12:13], 0, v[22:23]
	s_mov_b64 s[6:7], 0x20000
	s_waitcnt vmcnt(21)
; __device__ __forceinline__ unsigned f2bf(float f) { return cvt_pk_bf16_nat(f, 0.f) & 0xffffu; }
; __device__ __forceinline__ void xcd_barrier(const XcdBarrier& b) {
;     asm volatile("s_waitcnt vmcnt(0)" ::: "memory");
;     __syncthreads();
;     if (threadIdx.x == 0) {
;         unsigned* bar = b.bar;
;         __builtin_amdgcn_s_waitcnt(0);
;         unsigned nloc = b.st[0], nx = b.st[1];
;         if (nloc == 0u) { xcd_barrier_complete(bar, b.x, nloc, nx); b.st[0] = nloc; b.st[1] = nx; }
; __global__ void __launch_bounds__(NTHR, 2) mk_fwd(Args args) {
;     ...
;             LORAT[i] = (bf16)f2bf(v);
;         }
;         for (int i = hw * 64 + lane; i < 1024 * 256; i += HW * 64) {
;             const int n = i >> 8, c = i & 255, g = n >> 8, d = n & 255;
;             WPOOLT[i] = (bf16)f2bf(w_pool[((size_t)g * 256 + c) * 256 + d]);
	v_and_b32_e32 v100, v100, v120
	v_cvt_pk_bf16_f32 v100, v100, v100
	s_waitcnt vmcnt(20)
	v_and_b32_e32 v101, v101, v121
	v_cvt_pk_bf16_f32 v101, v101, v101
	s_waitcnt vmcnt(19)
	v_and_b32_e32 v102, v102, v122
	v_cvt_pk_bf16_f32 v102, v102, v102
	s_waitcnt vmcnt(18)
	v_and_b32_e32 v103, v103, v123
	v_cvt_pk_bf16_f32 v103, v103, v103
	s_waitcnt vmcnt(17)
	v_and_b32_e32 v104, v104, v124
	v_cvt_pk_bf16_f32 v104, v104, v104
	s_waitcnt vmcnt(16)
	v_and_b32_e32 v105, v105, v125
	v_cvt_pk_bf16_f32 v105, v105, v105
	s_waitcnt vmcnt(15)
	v_and_b32_e32 v106, v106, v126
	v_cvt_pk_bf16_f32 v106, v106, v106
	s_waitcnt vmcnt(14)
	v_and_b32_e32 v107, v107, v127
	v_cvt_pk_bf16_f32 v107, v107, v107
	s_waitcnt vmcnt(13)
	v_and_b32_e32 v108, v108, v128
	v_cvt_pk_bf16_f32 v108, v108, v108
	s_waitcnt vmcnt(12)
	v_and_b32_e32 v109, v109, v129
	v_cvt_pk_bf16_f32 v109, v109, v109
	s_waitcnt vmcnt(11)
	v_and_b32_e32 v110, v110, v130
	v_cvt_pk_bf16_f32 v110, v110, v110
	s_waitcnt vmcnt(10)
	v_and_b32_e32 v111, v111, v131
	v_cvt_pk_bf16_f32 v111, v111, v111
	s_waitcnt vmcnt(9)
	v_and_b32_e32 v112, v112, v132
	v_cvt_pk_bf16_f32 v112, v112, v112
	s_waitcnt vmcnt(8)
	v_and_b32_e32 v113, v113, v133
	v_cvt_pk_bf16_f32 v113, v113, v113
	s_waitcnt vmcnt(7)
	v_and_b32_e32 v114, v114, v134
	v_cvt_pk_bf16_f32 v114, v114, v114
	s_waitcnt vmcnt(6)
	v_and_b32_e32 v115, v115, v135
	v_cvt_pk_bf16_f32 v115, v115, v115
	s_waitcnt vmcnt(5)
	v_and_b32_e32 v116, v116, v136
	v_cvt_pk_bf16_f32 v116, v116, v116
	s_waitcnt vmcnt(4)
	v_and_b32_e32 v117, v117, v137
	v_cvt_pk_bf16_f32 v117, v117, v117
	s_waitcnt vmcnt(3)
	v_cvt_pk_bf16_f32 v140, v140, v140
	s_waitcnt vmcnt(2)
	v_cvt_pk_bf16_f32 v141, v141, v141
	s_waitcnt vmcnt(1)
	v_cvt_pk_bf16_f32 v142, v142, v142
	s_waitcnt vmcnt(0)
	v_cvt_pk_bf16_f32 v143, v143, v143
	global_store_short v[24:25], v100, off
	v_lshl_add_u64 v[24:25], v[24:25], 0, s[6:7]
	global_store_short v[24:25], v101, off
	v_lshl_add_u64 v[24:25], v[24:25], 0, s[6:7]
	global_store_short v[24:25], v102, off
	v_lshl_add_u64 v[24:25], v[24:25], 0, s[6:7]
	global_store_short v[24:25], v103, off
	v_lshl_add_u64 v[24:25], v[24:25], 0, s[6:7]
	global_store_short v[24:25], v104, off
	v_lshl_add_u64 v[24:25], v[24:25], 0, s[6:7]
	global_store_short v[24:25], v105, off
	v_lshl_add_u64 v[24:25], v[24:25], 0, s[6:7]
	global_store_short v[24:25], v106, off
	v_lshl_add_u64 v[24:25], v[24:25], 0, s[6:7]
	global_store_short v[24:25], v107, off
	v_lshl_add_u64 v[24:25], v[24:25], 0, s[6:7]
	global_store_short v[24:25], v108, off
	v_lshl_add_u64 v[24:25], v[24:25], 0, s[6:7]
	global_store_short v[24:25], v109, off
	v_lshl_add_u64 v[24:25], v[24:25], 0, s[6:7]
	global_store_short v[24:25], v110, off
	v_lshl_add_u64 v[24:25], v[24:25], 0, s[6:7]
	global_store_short v[24:25], v111, off
	v_lshl_add_u64 v[24:25], v[24:25], 0, s[6:7]
	global_store_short v[24:25], v112, off
	v_lshl_add_u64 v[24:25], v[24:25], 0, s[6:7]
	global_store_short v[24:25], v113, off
	v_lshl_add_u64 v[24:25], v[24:25], 0, s[6:7]
	global_store_short v[24:25], v114, off
	v_lshl_add_u64 v[24:25], v[24:25], 0, s[6:7]
	global_store_short v[24:25], v115, off
	v_lshl_add_u64 v[24:25], v[24:25], 0, s[6:7]
	global_store_short v[24:25], v116, off
	v_lshl_add_u64 v[24:25], v[24:25], 0, s[6:7]
	global_store_short v[24:25], v117, off
	v_lshl_add_u64 v[24:25], v[24:25], 0, s[6:7]
	global_store_short v[26:27], v140, off
	v_lshl_add_u64 v[26:27], v[26:27], 0, s[6:7]
	global_store_short v[26:27], v141, off
	v_lshl_add_u64 v[26:27], v[26:27], 0, s[6:7]
	global_store_short v[26:27], v142, off
	v_lshl_add_u64 v[26:27], v[26:27], 0, s[6:7]
	global_store_short v[26:27], v143, off
	v_lshl_add_u64 v[26:27], v[26:27], 0, s[6:7]
.LBB0_130:
.LBB0_131:
	s_cmp_gt_i32 s89, 2
	s_cselect_b64 s[0:1], -1, 0
	s_and_b64 s[2:3], s[4:5], s[0:1]
	s_andn2_b64 vcc, exec, s[2:3]
	s_cbranch_vccnz .LBB0_185
	s_waitcnt vmcnt(0)
	s_waitcnt vmcnt(0)
	s_barrier
	s_mov_b64 s[2:3], exec
	v_readlane_b32 s4, v252, 35
	v_readlane_b32 s5, v252, 36
	s_and_b64 s[4:5], s[2:3], s[4:5]
	s_mov_b64 exec, s[4:5]
	s_cbranch_execz .LBB0_184
	s_add_i32 s4, 0, 0x27020
	v_mov_b32_e32 v1, s4
	s_waitcnt vmcnt(0) expcnt(0) lgkmcnt(0)
	ds_read_b32 v3, v1
	s_add_i32 s4, 0, 0x27024
	v_mov_b32_e32 v1, s4
	ds_read_b32 v1, v1
	s_waitcnt lgkmcnt(1)
	v_cmp_ne_u32_e32 vcc, 0, v3
	s_cbranch_vccnz .LBB0_148
	v_readlane_b32 s4, v252, 32
	v_readlane_b32 s5, v252, 33
	s_load_dwordx2 s[8:9], s[4:5], 0x4
	s_add_u32 s4, s26, 0x4200
	s_addc_u32 s5, s27, 0
	s_add_u32 s6, s26, 0x4400
	s_addc_u32 s7, s27, 0
	s_waitcnt lgkmcnt(0)
	s_mul_i32 s29, s8, s33
	s_add_u32 s8, s26, 0x4500
	s_mul_i32 s29, s29, s9
	s_addc_u32 s9, s27, 0
	s_add_u32 s14, s26, 0x4600
	s_addc_u32 s15, s27, 0
	s_add_u32 s16, s26, 0x4700
	s_addc_u32 s17, s27, 0
	s_add_u32 s34, s26, 0x4800
	s_addc_u32 s35, s27, 0
	s_add_u32 s36, s26, 0x4900
	s_addc_u32 s37, s27, 0
	s_add_u32 s38, s26, 0x4a00
	s_addc_u32 s39, s27, 0
	s_add_u32 s40, s26, 0x4b00
	s_addc_u32 s41, s27, 0
	s_add_u32 s42, s26, 0x4c00
	s_addc_u32 s43, s27, 0
	s_add_u32 s44, s26, 0x4d00
	s_addc_u32 s45, s27, 0
	s_add_u32 s46, s26, 0x4e00
	s_addc_u32 s47, s27, 0
	s_add_u32 s48, s26, 0x4f00
	s_addc_u32 s49, s27, 0
	s_add_u32 s50, s26, 0x5000
	s_addc_u32 s51, s27, 0
	s_add_u32 s62, s26, 0x5100
	s_addc_u32 s63, s27, 0
	s_add_u32 s66, s26, 0x5200
	s_addc_u32 s67, s27, 0
	s_add_u32 s76, s26, 0x5300
	s_addc_u32 s77, s27, 0
	s_mov_b32 s31, 1
	v_mov_b32_e32 v17, 0
	s_branch .LBB0_136
